# layer-0 MLA loop hosts the 8192 MoE-0 down-weight conversion tasks (2-row slices per key tile, LDS hole staging); N2+ROUTER(0) drain halves
# speedup vs baseline: 1.0041x; 1.0041x over previous
.Lnoprio_a0:
	s_mov_b32 s98, 0
	s_mul_i32 s99, s82, 0x1400
	s_add_i32 s99, s99, 0x3400
	s_cmp_gt_u32 s82, 2
	s_cselect_b32 s0, 0x4400, 0
	s_add_i32 s99, s99, s0
	s_cmp_eq_u32 s82, 6
	s_cselect_b32 s99, 0x12800, s99
	s_cmp_eq_u32 s82, 7
	s_cselect_b32 s99, 0x16800, s99
	v_mov_b32_e32 v223, 0x204f8
	ds_read_b64 v[244:245], v223
	s_waitcnt lgkmcnt(0)
	v_readfirstlane_b32 s100, v244
	v_readfirstlane_b32 s101, v245
	s_mov_b32 s46, s15
	s_mov_b64 s[6:7], s[34:35]
	s_mov_b32 s41, s14
	s_add_i32 s0, 0, 0x20468
	s_add_u32 s8, s6, 0x58000
	v_mov_b32_e32 v0, s0
	s_addc_u32 s9, s7, 0
	s_add_i32 s0, 0, 0x204a0
	s_waitcnt lgkmcnt(0)
	v_mov_b32_e32 v2, s0
	s_add_i32 s0, 0, 0x20488
	s_waitcnt vmcnt(0)
	v_mov_b32_e32 v4, s0
	ds_read_b64 v[0:1], v0
	ds_read_b64 v[2:3], v2
	ds_read_b64 v[4:5], v4
	v_readfirstlane_b32 s47, v184
	s_cmpk_lt_i32 s41, 0x110
	s_cselect_b64 s[12:13], -1, 0
	s_and_b32 s0, s47, 0xffffffc0
	s_mov_b32 s16, 0
	s_waitcnt lgkmcnt(2)
	v_readfirstlane_b32 s10, v0
	v_readfirstlane_b32 s11, v1
	s_waitcnt lgkmcnt(1)
	v_readfirstlane_b32 s48, v2
	v_readfirstlane_b32 s49, v3
	s_waitcnt lgkmcnt(0)
	v_readfirstlane_b32 s38, v4
	v_readfirstlane_b32 s39, v5
	s_cmpk_gt_i32 s41, 0x10f
	v_add_u32_e32 v200, s0, v193
	s_cbranch_scc1 .LBB0_598
	s_add_u32 s50, s6, 0x4619c000
	s_addc_u32 s51, s7, 0
	s_add_u32 s52, s6, 0x49d1c000
	s_addc_u32 s53, s7, 0
	s_add_u32 s54, s6, 0x216b8000
	s_addc_u32 s55, s7, 0
	s_add_u32 s56, s6, 0x37e0c000
	s_addc_u32 s57, s7, 0
	s_movk_i32 s58, 0xff
	s_movk_i32 s59, 0x100
	s_movk_i32 s60, 0x2000
	s_movk_i32 s61, 0xc00
	v_mov_b32_e32 v187, 0
	v_mov_b32_e32 v185, 0x358637bd
	s_mov_b32 s62, 0x800000
	s_mov_b32 s63, 0x2aaaaaab
	s_movk_i32 s64, 0x600
	s_movk_i32 s65, 0xd0
	s_movk_i32 s66, 0x50
	s_add_i32 s67, 0, 0x10000
	s_mov_b32 s68, 0xaaaaaaab
	s_mov_b32 s69, 0xc3e00000
	v_mov_b32_e32 v201, 0x7149f2ca
	s_mov_b32 s40, 0x3dd53b94
	s_mov_b32 s70, 0x41000000
	v_mov_b32_e32 v202, 0xc0a00000
	v_mov_b32_e32 v203, 0x43e00000
	v_mov_b32_e32 v204, 0xf149f2ca
	s_mov_b32 s71, s41
	s_branch .LBB0_548

.LBB0_563:
	s_or_b64 exec, exec, s[2:3]
	v_mul_f32_e32 v0, v108, v0
	v_mul_f32_e32 v1, v108, v1
	v_mul_f32_e32 v27, v108, v27
	v_mul_f32_e32 v0, v0, v114
	v_mul_f32_e32 v1, v1, v113
	v_mul_f32_e32 v27, v27, v135
	v_med3_f32 v0, v0, s69, v203
	v_med3_f32 v1, v1, s69, v203
	v_mov_b32_e32 v135, v187
	v_cvt_pk_fp8_f32 v135, v0, v1
	v_mul_f32_e32 v2, v108, v2
	v_mul_f32_e32 v3, v108, v3
	v_mul_f32_e32 v2, v2, v112
	v_mul_f32_e32 v3, v3, v111
	v_med3_f32 v0, v2, s69, v203
	v_med3_f32 v1, v3, s69, v203
	v_mul_f32_e32 v26, v108, v26
	v_cvt_pk_fp8_f32 v135, v0, v1 op_sel:[0,0,1]
	v_max_f32_e32 v0, v106, v106
	v_max_f32_e32 v1, v107, v107
	v_mul_f32_e32 v26, v26, v136
	v_med3_f32 v0, v0, s69, v203
	v_med3_f32 v1, v1, s69, v203
	v_mov_b32_e32 v136, v187
	v_cvt_pk_fp8_f32 v136, v0, v1
	v_max_f32_e32 v2, v102, v102
	v_max_f32_e32 v1, v103, v103
	v_med3_f32 v0, v2, s69, v203
	v_med3_f32 v1, v1, s69, v203
	v_mul_f32_e32 v25, v108, v25
	v_cvt_pk_fp8_f32 v136, v0, v1 op_sel:[0,0,1]
	v_max_f32_e32 v0, v100, v100
	v_max_f32_e32 v1, v101, v101
	v_mul_f32_e32 v25, v25, v137
	v_med3_f32 v0, v0, s69, v203
	v_med3_f32 v1, v1, s69, v203
	v_mov_b32_e32 v137, v187
	v_cvt_pk_fp8_f32 v137, v0, v1
	v_max_f32_e32 v2, v98, v98
	v_max_f32_e32 v1, v99, v99
	v_med3_f32 v0, v2, s69, v203
	v_med3_f32 v1, v1, s69, v203
	v_mul_f32_e32 v24, v108, v24
	v_cvt_pk_fp8_f32 v137, v0, v1 op_sel:[0,0,1]
	v_max_f32_e32 v0, v96, v96
	v_max_f32_e32 v1, v97, v97
	v_mul_f32_e32 v24, v24, v138
	v_med3_f32 v0, v0, s69, v203
	v_med3_f32 v1, v1, s69, v203
	v_mov_b32_e32 v138, v187
	v_cvt_pk_fp8_f32 v138, v0, v1
	v_max_f32_e32 v2, v94, v94
	v_max_f32_e32 v1, v95, v95
	v_med3_f32 v0, v2, s69, v203
	v_med3_f32 v1, v1, s69, v203
	v_mul_f32_e32 v31, v108, v31
	v_cvt_pk_fp8_f32 v138, v0, v1 op_sel:[0,0,1]
	v_max_f32_e32 v0, v92, v92
	v_max_f32_e32 v1, v93, v93
	v_mul_f32_e32 v31, v31, v139
	v_med3_f32 v0, v0, s69, v203
	v_med3_f32 v1, v1, s69, v203
	v_mov_b32_e32 v139, v187
	v_cvt_pk_fp8_f32 v139, v0, v1
	v_max_f32_e32 v2, v90, v90
	v_max_f32_e32 v1, v91, v91
	v_med3_f32 v0, v2, s69, v203
	v_med3_f32 v1, v1, s69, v203
	v_mul_f32_e32 v30, v108, v30
	v_cvt_pk_fp8_f32 v139, v0, v1 op_sel:[0,0,1]
	v_max_f32_e32 v0, v88, v88
	v_max_f32_e32 v1, v89, v89
	v_mul_f32_e32 v30, v30, v140
	v_med3_f32 v0, v0, s69, v203
	v_med3_f32 v1, v1, s69, v203
	v_mov_b32_e32 v140, v187
	v_cvt_pk_fp8_f32 v140, v0, v1
	v_max_f32_e32 v2, v86, v86
	v_max_f32_e32 v1, v87, v87
	v_med3_f32 v0, v2, s69, v203
	v_med3_f32 v1, v1, s69, v203
	v_mul_f32_e32 v29, v108, v29
	v_cvt_pk_fp8_f32 v140, v0, v1 op_sel:[0,0,1]
	v_max_f32_e32 v0, v84, v84
	v_max_f32_e32 v1, v85, v85
	v_mul_f32_e32 v29, v29, v141
	v_med3_f32 v0, v0, s69, v203
	v_med3_f32 v1, v1, s69, v203
	v_mov_b32_e32 v141, v187
	v_cvt_pk_fp8_f32 v141, v0, v1
	v_max_f32_e32 v2, v82, v82
	v_max_f32_e32 v1, v83, v83
	v_med3_f32 v0, v2, s69, v203
	v_med3_f32 v1, v1, s69, v203
	v_mul_f32_e32 v28, v108, v28
	v_cvt_pk_fp8_f32 v141, v0, v1 op_sel:[0,0,1]
	v_max_f32_e32 v0, v80, v80
	v_max_f32_e32 v1, v81, v81
	v_mul_f32_e32 v28, v28, v142
	v_med3_f32 v0, v0, s69, v203
	v_med3_f32 v1, v1, s69, v203
	v_mov_b32_e32 v142, v187
	v_cvt_pk_fp8_f32 v142, v0, v1
	v_mul_f32_e32 v4, v108, v4
	v_mul_f32_e32 v5, v108, v5
	v_mul_f32_e32 v60, v60, v108
	v_mul_f32_e32 v61, v61, v108
	v_mul_f32_e32 v56, v56, v108
	v_mul_f32_e32 v57, v57, v108
	v_mul_f32_e32 v52, v52, v108
	v_mul_f32_e32 v53, v108, v53
	v_mul_f32_e32 v48, v108, v48
	v_mul_f32_e32 v49, v108, v49
	v_mul_f32_e32 v44, v108, v44
	v_mul_f32_e32 v45, v108, v45
	v_mul_f32_e32 v40, v108, v40
	v_mul_f32_e32 v41, v108, v41
	v_mul_f32_e32 v36, v108, v36
	v_mul_f32_e32 v37, v108, v37
	v_mul_f32_e32 v32, v108, v32
	v_mul_f32_e32 v33, v108, v33
	v_mul_f32_e32 v20, v108, v20
	v_mul_f32_e32 v4, v4, v118
	v_mul_f32_e32 v5, v5, v117
	v_max_f32_e32 v2, v78, v78
	v_max_f32_e32 v1, v79, v79
	v_mul_f32_e32 v60, v60, v182
	v_mul_f32_e32 v61, v61, v181
	v_mul_f32_e32 v56, v56, v178
	v_mul_f32_e32 v57, v57, v177
	v_mul_f32_e32 v52, v52, v174
	v_mul_f32_e32 v53, v53, v173
	v_mul_f32_e32 v48, v48, v162
	v_mul_f32_e32 v49, v49, v161
	v_mul_f32_e32 v44, v44, v158
	v_mul_f32_e32 v45, v45, v157
	v_mul_f32_e32 v40, v40, v154
	v_mul_f32_e32 v41, v41, v153
	v_mul_f32_e32 v36, v36, v150
	v_mul_f32_e32 v37, v37, v149
	v_mul_f32_e32 v32, v32, v146
	v_mul_f32_e32 v33, v33, v145
	v_mul_f32_e32 v20, v20, v134
	v_mul_f32_e32 v19, v108, v19
	v_mul_f32_e32 v12, v108, v12
	v_mul_f32_e32 v13, v108, v13
	v_mul_f32_e32 v14, v108, v14
	v_mul_f32_e32 v15, v108, v15
	v_mul_f32_e32 v8, v108, v8
	v_mul_f32_e32 v9, v108, v9
	v_mul_f32_e32 v10, v108, v10
	v_med3_f32 v4, v4, s69, v203
	v_med3_f32 v5, v5, s69, v203
	v_mov_b32_e32 v134, v187
	v_med3_f32 v0, v2, s69, v203
	v_med3_f32 v1, v1, s69, v203
	v_mul_f32_e32 v35, v108, v35
	v_mul_f32_e32 v21, v108, v21
	v_mul_f32_e32 v19, v19, v127
	v_mul_f32_e32 v12, v12, v126
	v_mul_f32_e32 v13, v13, v125
	v_mul_f32_e32 v14, v14, v124
	v_mul_f32_e32 v15, v15, v123
	v_mul_f32_e32 v8, v8, v122
	v_mul_f32_e32 v9, v9, v121
	v_mul_f32_e32 v10, v10, v120
	v_med3_f32 v60, v60, s69, v203
	v_med3_f32 v61, v61, s69, v203
	v_mov_b32_e32 v120, v187
	v_med3_f32 v56, v56, s69, v203
	v_med3_f32 v57, v57, s69, v203
	v_mov_b32_e32 v121, v187
	v_med3_f32 v52, v52, s69, v203
	v_med3_f32 v53, v53, s69, v203
	v_mov_b32_e32 v122, v187
	v_med3_f32 v48, v48, s69, v203
	v_med3_f32 v49, v49, s69, v203
	v_mov_b32_e32 v123, v187
	v_med3_f32 v44, v44, s69, v203
	v_med3_f32 v45, v45, s69, v203
	v_mov_b32_e32 v124, v187
	v_med3_f32 v40, v40, s69, v203
	v_med3_f32 v41, v41, s69, v203
	v_mov_b32_e32 v125, v187
	v_med3_f32 v36, v36, s69, v203
	v_med3_f32 v37, v37, s69, v203
	v_mov_b32_e32 v126, v187
	v_med3_f32 v32, v32, s69, v203
	v_med3_f32 v33, v33, s69, v203
	v_mov_b32_e32 v127, v187
	v_cvt_pk_fp8_f32 v134, v4, v5
	v_cvt_pk_fp8_f32 v142, v0, v1 op_sel:[0,0,1]
	v_max_f32_e32 v0, v76, v76
	v_max_f32_e32 v1, v77, v77
	v_mul_f32_e32 v35, v35, v143
	v_mul_f32_e32 v21, v21, v133
	v_mul_f32_e32 v6, v108, v6
	v_mul_f32_e32 v7, v108, v7
	v_cvt_pk_fp8_f32 v120, v60, v61
	v_cvt_pk_fp8_f32 v121, v56, v57
	v_cvt_pk_fp8_f32 v122, v52, v53
	v_cvt_pk_fp8_f32 v123, v48, v49
	v_cvt_pk_fp8_f32 v124, v44, v45
	v_cvt_pk_fp8_f32 v125, v40, v41
	v_cvt_pk_fp8_f32 v126, v36, v37
	v_cvt_pk_fp8_f32 v127, v32, v33
	v_med3_f32 v8, v8, s69, v203
	v_med3_f32 v9, v9, s69, v203
	v_mov_b32_e32 v133, v187
	v_med3_f32 v0, v0, s69, v203
	v_med3_f32 v1, v1, s69, v203
	v_mov_b32_e32 v143, v187
	v_mul_f32_e32 v62, v62, v108
	v_mul_f32_e32 v63, v63, v108
	v_mul_f32_e32 v58, v58, v108
	v_mul_f32_e32 v59, v59, v108
	v_mul_f32_e32 v54, v108, v54
	v_mul_f32_e32 v55, v108, v55
	v_mul_f32_e32 v50, v108, v50
	v_mul_f32_e32 v51, v108, v51
	v_mul_f32_e32 v46, v108, v46
	v_mul_f32_e32 v47, v108, v47
	v_mul_f32_e32 v42, v108, v42
	v_mul_f32_e32 v43, v108, v43
	v_mul_f32_e32 v38, v108, v38
	v_mul_f32_e32 v39, v108, v39
	v_mul_f32_e32 v34, v108, v34
	v_mul_f32_e32 v16, v108, v16
	v_mul_f32_e32 v17, v108, v17
	v_mul_f32_e32 v6, v6, v116
	v_mul_f32_e32 v7, v7, v115
	v_cvt_pk_fp8_f32 v133, v8, v9
	v_cvt_pk_fp8_f32 v143, v0, v1
	v_mul_u32_u24_e32 v0, 0xd0, v186
	s_and_b32 s3, s17, 0x3fffffc0
	v_mul_f32_e32 v62, v62, v180
	v_mul_f32_e32 v63, v63, v179
	v_mul_f32_e32 v58, v58, v176
	v_mul_f32_e32 v59, v59, v175
	v_mul_f32_e32 v54, v54, v172
	v_mul_f32_e32 v55, v55, v163
	v_mul_f32_e32 v50, v50, v160
	v_mul_f32_e32 v51, v51, v159
	v_mul_f32_e32 v46, v46, v156
	v_mul_f32_e32 v47, v47, v155
	v_mul_f32_e32 v42, v42, v152
	v_mul_f32_e32 v43, v43, v151
	v_mul_f32_e32 v38, v38, v148
	v_mul_f32_e32 v39, v39, v147
	v_mul_f32_e32 v34, v34, v144
	v_mul_f32_e32 v23, v108, v23
	v_mul_f32_e32 v16, v16, v130
	v_mul_f32_e32 v17, v17, v129
	v_mul_f32_e32 v18, v108, v18
	v_mul_f32_e32 v11, v108, v11
	v_med3_f32 v6, v6, s69, v203
	v_med3_f32 v7, v7, s69, v203
	v_add3_u32 v216, 0, v0, v72
	s_lshl_b32 s3, s3, 2
	s_ashr_i32 s18, s18, 6
	v_mul_f32_e32 v23, v23, v131
	v_mul_f32_e32 v18, v18, v128
	v_mul_f32_e32 v11, v11, v119
	v_med3_f32 v62, v62, s69, v203
	v_med3_f32 v63, v63, s69, v203
	v_med3_f32 v56, v58, s69, v203
	v_med3_f32 v57, v59, s69, v203
	v_med3_f32 v54, v54, s69, v203
	v_med3_f32 v55, v55, s69, v203
	v_med3_f32 v48, v50, s69, v203
	v_med3_f32 v49, v51, s69, v203
	v_med3_f32 v46, v46, s69, v203
	v_med3_f32 v47, v47, s69, v203
	v_med3_f32 v40, v42, s69, v203
	v_med3_f32 v41, v43, s69, v203
	v_med3_f32 v38, v38, s69, v203
	v_med3_f32 v39, v39, s69, v203
	v_med3_f32 v32, v34, s69, v203
	v_med3_f32 v33, v35, s69, v203
	v_med3_f32 v28, v28, s69, v203
	v_med3_f32 v29, v29, s69, v203
	v_mov_b32_e32 v128, v187
	v_med3_f32 v24, v24, s69, v203
	v_med3_f32 v25, v25, s69, v203
	v_mov_b32_e32 v129, v187
	v_med3_f32 v20, v20, s69, v203
	v_med3_f32 v21, v21, s69, v203
	v_mov_b32_e32 v130, v187
	v_med3_f32 v16, v16, s69, v203
	v_med3_f32 v17, v17, s69, v203
	v_mov_b32_e32 v131, v187
	v_cvt_pk_fp8_f32 v134, v6, v7 op_sel:[0,0,1]
	ds_read_b128 v[0:3], v216
	ds_read_b128 v[4:7], v216 offset:16
	s_add_i32 s3, s3, 0
	s_ashr_i32 s19, s18, 31
	s_lshl_b32 s2, s74, 1
	v_cvt_pk_fp8_f32 v120, v62, v63 op_sel:[0,0,1]
	v_cvt_pk_fp8_f32 v121, v56, v57 op_sel:[0,0,1]
	v_cvt_pk_fp8_f32 v122, v54, v55 op_sel:[0,0,1]
	v_cvt_pk_fp8_f32 v123, v48, v49 op_sel:[0,0,1]
	v_cvt_pk_fp8_f32 v124, v46, v47 op_sel:[0,0,1]
	v_cvt_pk_fp8_f32 v125, v40, v41 op_sel:[0,0,1]
	v_cvt_pk_fp8_f32 v126, v38, v39 op_sel:[0,0,1]
	v_cvt_pk_fp8_f32 v127, v32, v33 op_sel:[0,0,1]
	v_cvt_pk_fp8_f32 v128, v28, v29
	v_cvt_pk_fp8_f32 v129, v24, v25
	v_cvt_pk_fp8_f32 v130, v20, v21
	v_cvt_pk_fp8_f32 v131, v16, v17
	v_med3_f32 v8, v10, s69, v203
	v_med3_f32 v9, v11, s69, v203
	s_add_i32 s79, s3, 0x18000
	s_lshl_b64 s[18:19], s[18:19], 16
	v_mul_f32_e32 v22, v108, v22
	v_cvt_pk_fp8_f32 v133, v8, v9 op_sel:[0,0,1]
	v_max_f32_e32 v8, v74, v74
	v_max_f32_e32 v9, v75, v75
	s_add_u32 s18, s44, s18
	v_mul_f32_e32 v22, v22, v132
	v_med3_f32 v8, v8, s69, v203
	v_med3_f32 v9, v9, s69, v203
	s_addc_u32 s19, s45, s19
	v_med3_f32 v30, v30, s69, v203
	v_med3_f32 v31, v31, s69, v203
	v_med3_f32 v24, v26, s69, v203
	v_med3_f32 v25, v27, s69, v203
	v_med3_f32 v22, v22, s69, v203
	v_med3_f32 v23, v23, s69, v203
	v_med3_f32 v16, v18, s69, v203
	v_med3_f32 v17, v19, s69, v203
	v_cvt_pk_fp8_f32 v143, v8, v9 op_sel:[0,0,1]
	v_lshl_add_u64 v[8:9], s[18:19], 0, v[104:105]
	v_cvt_pk_fp8_f32 v128, v30, v31 op_sel:[0,0,1]
	v_cvt_pk_fp8_f32 v129, v24, v25 op_sel:[0,0,1]
	v_cvt_pk_fp8_f32 v130, v22, v23 op_sel:[0,0,1]
	v_cvt_pk_fp8_f32 v131, v16, v17 op_sel:[0,0,1]
	s_waitcnt lgkmcnt(0)
	v_mfma_scale_f32_32x32x64_f8f6f4 v[16:31], v[0:7], v[120:127], 0, v205, v205 op_sel_hi:[0,0,0]
	ds_read_b128 v[0:3], v216 offset:64
	ds_read_b128 v[4:7], v216 offset:80
	global_load_dwordx4 v[172:175], v[8:9], off
	v_med3_f32 v12, v12, s69, v203
	v_med3_f32 v13, v13, s69, v203
	v_mov_b32_e32 v132, v187
	v_cvt_pk_fp8_f32 v132, v12, v13
	v_med3_f32 v14, v14, s69, v203
	v_med3_f32 v15, v15, s69, v203
	s_mov_b32 s17, s16
	v_cvt_pk_fp8_f32 v132, v14, v15 op_sel:[0,0,1]
	s_mov_b32 s18, s16
	s_mov_b32 s19, s16
	s_mov_b32 s20, s16
	s_mov_b32 s21, s16
	s_mov_b32 s22, s16
	s_waitcnt lgkmcnt(0)
	v_mfma_scale_f32_32x32x64_f8f6f4 v[16:31], v[0:7], v[128:135], v[16:31], v205, v205 op_sel_hi:[0,0,0]
	v_sub_u32_e32 v0, v216, v73
	ds_read_b128 v[32:35], v0 offset:128
	ds_read_b128 v[36:39], v0 offset:160
	s_mov_b32 s23, s16
	s_mov_b32 s24, s16
	s_mov_b32 s25, s16
	s_mov_b32 s26, s16
	s_mov_b32 s27, s16
	s_mov_b32 s28, s16
	s_mov_b32 s29, s16
	s_mov_b32 s30, s16
	s_mov_b32 s31, s16
	v_mov_b64_e32 v[0:1], s[16:17]
	v_and_b32_e32 v64, 63, v110
	v_mov_b64_e32 v[14:15], s[30:31]
	v_mov_b64_e32 v[2:3], s[18:19]
	s_waitcnt lgkmcnt(0)
	v_mfma_scale_f32_32x32x64_f8f6f4 v[16:31], v[32:39], v[136:143], v[16:31], v205, v205 op_sel_hi:[0,0,0]
	v_mov_b64_e32 v[4:5], s[20:21]
	v_mov_b64_e32 v[6:7], s[22:23]
	v_mov_b64_e32 v[8:9], s[24:25]
	v_mov_b64_e32 v[10:11], s[26:27]
	v_mov_b64_e32 v[12:13], s[28:29]
	v_sub_u32_e32 v217, 0, v73
	v_mov_b32_e32 v112, 0x38383838
	v_mov_b64_e32 v[62:63], v[14:15]
	s_mov_b32 s78, 2
	v_lshl_add_u32 v209, v186, 2, s79
	v_mov_b32_e32 v113, v112
	v_mov_b32_e32 v114, v112
	v_mov_b32_e32 v115, v112
	v_mov_b32_e32 v116, v112
	s_nop 5
	v_max_f32_e32 v32, v16, v17
	v_max3_f32 v32, v32, v18, v19
	v_max3_f32 v32, v32, v20, v21
	v_max3_f32 v32, v32, v22, v23
	v_max3_f32 v32, v32, v24, v25
	v_max3_f32 v32, v32, v26, v27
	v_max3_f32 v32, v32, v28, v29
	v_max3_f32 v32, v32, v30, v31
	v_mov_b32_e32 v33, v32
	s_nop 1
	v_permlane32_swap_b32_e32 v32, v33
	v_max_f32_e32 v32, v32, v33
	v_fmamk_f32 v33, v32, 0x3dd53b94, v201
	v_fmamk_f32 v32, v32, 0x3dd53b94, v202
	v_max_f32_e32 v32, 0xf149f2ca, v32
	v_cmp_ge_f32_e32 vcc, s70, v33
	v_sub_f32_e32 v33, 0xf149f2ca, v32
	s_cmp_eq_u64 vcc, exec
	v_exp_f32_e32 v33, v33
	s_cselect_b64 vcc, -1, 0
	v_cndmask_b32_e32 v192, v32, v204, vcc
	v_pk_fma_f32 v[178:179], v[16:17], s[40:41], v[192:193] op_sel_hi:[1,0,0] neg_lo:[0,0,1] neg_hi:[0,0,1]
	v_mul_u32_u24_e32 v16, 0x50, v186
	v_pk_fma_f32 v[152:153], v[30:31], s[40:41], v[192:193] op_sel_hi:[1,0,0] neg_lo:[0,0,1] neg_hi:[0,0,1]
	v_pk_fma_f32 v[154:155], v[28:29], s[40:41], v[192:193] op_sel_hi:[1,0,0] neg_lo:[0,0,1] neg_hi:[0,0,1]
	v_pk_fma_f32 v[156:157], v[26:27], s[40:41], v[192:193] op_sel_hi:[1,0,0] neg_lo:[0,0,1] neg_hi:[0,0,1]
	v_pk_fma_f32 v[158:159], v[24:25], s[40:41], v[192:193] op_sel_hi:[1,0,0] neg_lo:[0,0,1] neg_hi:[0,0,1]
	v_pk_fma_f32 v[160:161], v[22:23], s[40:41], v[192:193] op_sel_hi:[1,0,0] neg_lo:[0,0,1] neg_hi:[0,0,1]
	v_pk_fma_f32 v[162:163], v[20:21], s[40:41], v[192:193] op_sel_hi:[1,0,0] neg_lo:[0,0,1] neg_hi:[0,0,1]
	v_pk_fma_f32 v[176:177], v[18:19], s[40:41], v[192:193] op_sel_hi:[1,0,0] neg_lo:[0,0,1] neg_hi:[0,0,1]
	v_cndmask_b32_e64 v88, v33, 1.0, vcc
	v_add3_u32 v211, s67, v16, v72
	s_add_i32 s17, s2, -2
	v_cmp_gt_u32_e64 s[2:3], 32, v64
	v_mov_b64_e32 v[30:31], v[14:15]
	v_mov_b64_e32 v[46:47], v[14:15]
	v_mov_b64_e32 v[78:79], v[14:15]
	v_mov_b32_e32 v117, v112
	v_mov_b32_e32 v118, v112
	v_mov_b32_e32 v119, v112
	v_lshlrev_b32_e32 v208, 2, v109
	v_mul_lo_u32 v215, v213, s65
	v_lshl_add_u32 v214, v109, 4, s79
	s_add_i32 s20, s74, -1
	v_lshl_add_u64 v[194:195], s[4:5], 0, v[190:191]
	v_lshl_add_u64 v[196:197], s[4:5], 0, v[188:189]
	v_lshl_add_u64 v[198:199], s[44:45], 0, v[104:105]
	s_mov_b32 s21, 0
	s_movk_i32 s22, 0x80
	v_mov_b64_e32 v[28:29], v[12:13]
	v_mov_b64_e32 v[26:27], v[10:11]
	v_mov_b64_e32 v[24:25], v[8:9]
	v_mov_b64_e32 v[22:23], v[6:7]
	v_mov_b64_e32 v[20:21], v[4:5]
	v_mov_b64_e32 v[18:19], v[2:3]
	v_mov_b64_e32 v[16:17], v[0:1]
	v_mov_b64_e32 v[44:45], v[12:13]
	v_mov_b64_e32 v[42:43], v[10:11]
	v_mov_b64_e32 v[40:41], v[8:9]
	v_mov_b64_e32 v[38:39], v[6:7]
	v_mov_b64_e32 v[36:37], v[4:5]
	v_mov_b64_e32 v[34:35], v[2:3]
	v_mov_b64_e32 v[32:33], v[0:1]
	v_mov_b64_e32 v[60:61], v[12:13]
	v_mov_b64_e32 v[58:59], v[10:11]
	v_mov_b64_e32 v[56:57], v[8:9]
	v_mov_b64_e32 v[54:55], v[6:7]
	v_mov_b64_e32 v[52:53], v[4:5]
	v_mov_b64_e32 v[50:51], v[2:3]
	v_mov_b64_e32 v[48:49], v[0:1]
	v_mov_b64_e32 v[76:77], v[12:13]
	v_mov_b64_e32 v[74:75], v[10:11]
	v_mov_b64_e32 v[72:73], v[8:9]
	v_mov_b64_e32 v[70:71], v[6:7]
	v_mov_b64_e32 v[68:69], v[4:5]
	v_mov_b64_e32 v[66:67], v[2:3]
	v_mov_b64_e32 v[64:65], v[0:1]
	v_mbcnt_hi_u32_b32 v223, -1, v253
	v_and_b32_e32 v241, 15, v223
	v_lshlrev_b32_e32 v241, 4, v241
	v_lshrrev_b32_e32 v242, 4, v223
	v_lshl_or_b32 v241, v242, 17, v241
	v_add_u32_e32 v242, 0x2000, v241
	global_load_dwordx4 v[244:247], v241, s[100:101] nt
	global_load_dwordx4 v[248:251], v242, s[100:101] nt
	s_branch .LBB0_566

.LBB0_570:
	s_waitcnt lgkmcnt(4)
	v_mfma_scale_f32_32x32x64_f8f6f4 v[80:95], v[80:87], v[120:127], 0, v205, v205 op_sel_hi:[0,0,0]
	s_mov_b64 s[4:5], exec
	s_cmp_ge_u32 s18, s20
	s_waitcnt lgkmcnt(2)
	v_mfma_scale_f32_32x32x64_f8f6f4 v[80:95], v[104:111], v[128:135], v[80:95], v205, v205 op_sel_hi:[0,0,0]
	s_waitcnt lgkmcnt(0)
	v_mfma_scale_f32_32x32x64_f8f6f4 v[80:95], v[96:103], v[136:143], v[80:95], v205, v205 op_sel_hi:[0,0,0]
	s_nop 15
	s_nop 3
	v_max_f32_e32 v96, v80, v81
	v_max3_f32 v96, v96, v82, v83
	v_max3_f32 v96, v96, v84, v85
	v_max3_f32 v96, v96, v86, v87
	v_max3_f32 v96, v96, v88, v89
	v_max3_f32 v96, v96, v90, v91
	v_max3_f32 v96, v96, v92, v93
	v_max3_f32 v96, v96, v94, v95
	v_mov_b32_e32 v97, v96
	s_nop 1
	v_permlane32_swap_b32_e32 v96, v97
	v_max_f32_e32 v96, v96, v97
	v_fma_f32 v97, v96, s40, -v192
	v_cmp_ge_f32_e32 vcc, s70, v97
	s_cbranch_scc1 .LBB0_577
	s_xor_b32 s25, s23, 1
	s_lshl_b32 s18, s25, 15
	s_add_i32 s26, s18, 0
	v_add3_u32 v97, s26, v212, v190
	s_waitcnt vmcnt(3)
	ds_write_b128 v97, v[168:171]
	s_and_saveexec_b64 s[18:19], s[0:1]
	v_add3_u32 v97, s26, v215, v188
	ds_write_b128 v97, v[164:167]
	s_or_b64 exec, exec, s[18:19]
	v_lshl_add_u32 v97, s25, 14, v207
	s_cmp_ge_u32 s78, s74
	s_waitcnt vmcnt(2)
	ds_write_b128 v97, v[172:175]
	s_waitcnt vmcnt(0)
	s_cmp_gt_u32 s98, 35
	s_cbranch_scc1 .Lcv_done_0
	s_mul_i32 s18, s98, 57
	s_lshr_b32 s18, s18, 9
	s_mul_i32 s19, s18, 9
	s_sub_i32 s19, s98, s19
	s_cmp_eq_u32 s19, 0
	s_cbranch_scc1 .Lcv_setup_0
	v_mul_f32_e32 v244, 0x42000000, v244
	v_mul_f32_e32 v245, 0x42000000, v245
	v_mul_f32_e32 v246, 0x42000000, v246
	v_mul_f32_e32 v247, 0x42000000, v247
	v_mul_f32_e32 v248, 0x42000000, v248
	v_mul_f32_e32 v249, 0x42000000, v249
	v_mul_f32_e32 v250, 0x42000000, v250
	v_mul_f32_e32 v251, 0x42000000, v251
	v_med3_f32 v244, v244, s69, v203
	v_med3_f32 v245, v245, s69, v203
	v_med3_f32 v246, v246, s69, v203
	v_med3_f32 v247, v247, s69, v203
	v_med3_f32 v248, v248, s69, v203
	v_med3_f32 v249, v249, s69, v203
	v_med3_f32 v250, v250, s69, v203
	v_med3_f32 v251, v251, s69, v203
	v_cvt_pk_fp8_f32 v244, v244, v248
	v_cvt_pk_fp8_f32 v245, v245, v249
	v_cvt_pk_fp8_f32 v246, v246, v250
	v_cvt_pk_fp8_f32 v247, v247, v251
	s_nop 0
	ds_write_b16 v243, v244
	ds_write_b16 v243, v245 offset:80
	ds_write_b16 v243, v246 offset:160
	ds_write_b16 v243, v247 offset:240
	v_add_u32_e32 v243, 2, v243
	s_cmp_eq_u32 s19, 8
	s_cbranch_scc1 .Lcv_store_0
	s_add_u32 s100, s100, 0x4000
	s_addc_u32 s101, s101, 0
	s_branch .Lcv_next_0
.Lcv_setup_0:
	s_lshl_b32 s25, s14, 3
	s_add_i32 s25, s25, s82
	s_lshr_b32 s26, s25, 6
	s_and_b32 s25, s25, 63
	s_lshl_b32 s25, s25, 2
	s_add_i32 s25, s25, s18
	v_mov_b32_e32 v223, 0x204f8
	ds_read_b64 v[244:245], v223
	s_and_b32 s27, s25, 7
	s_lshl_b32 s27, s27, 19
	s_lshr_b32 s19, s25, 3
	s_lshl_b32 s19, s19, 8
	s_add_i32 s27, s27, s19
	s_lshl_b32 s26, s26, 22
	s_add_i32 s26, s26, s27
	s_waitcnt lgkmcnt(0)
	v_readfirstlane_b32 s100, v244
	v_readfirstlane_b32 s101, v245
	v_bfe_u32 v243, v241, 4, 4
	v_mul_u32_u24_e32 v243, 0x140, v243
	v_lshrrev_b32_e32 v223, 17, v241
	v_lshl_add_u32 v243, v223, 4, v243
	v_add_u32_e32 v243, s99, v243
	s_add_u32 s100, s100, s26
	s_addc_u32 s101, s101, 0
	s_branch .Lcv_next_0
.Lcv_store_0:
	s_lshl_b32 s25, s14, 3
	s_add_i32 s25, s25, s82
	s_lshr_b32 s26, s25, 6
	s_and_b32 s25, s25, 63
	s_lshl_b32 s25, s25, 2
	s_add_i32 s25, s25, s18
	s_and_b32 s27, s25, 7
	s_lshl_b32 s27, s27, 6
	s_lshr_b32 s19, s25, 3
	s_lshl_b32 s19, s19, 15
	s_add_i32 s27, s27, s19
	s_lshl_b32 s26, s26, 20
	s_add_i32 s25, s27, s26
	s_add_u32 s26, s34, 0x17458000
	s_addc_u32 s27, s35, 0
	s_add_u32 s26, s26, s25
	s_addc_u32 s27, s27, 0
	v_mbcnt_hi_u32_b32 v252, -1, v253
	v_lshrrev_b32_e32 v223, 2, v252
	v_and_b32_e32 v252, 3, v252
	v_lshlrev_b32_e32 v252, 4, v252
	v_mul_u32_u24_e32 v244, 0x50, v223
	v_lshl_add_u32 v223, v223, 9, v252
	v_add3_u32 v252, v244, v252, s99
	s_waitcnt lgkmcnt(0)
	ds_read_b128 v[244:247], v252
	ds_read_b128 v[248:251], v252 offset:1280
	s_waitcnt lgkmcnt(0)
	global_store_dwordx4 v223, v[244:247], s[26:27]
	s_add_u32 s26, s26, 0x2000
	s_addc_u32 s27, s27, 0
	s_nop 0
	global_store_dwordx4 v223, v[248:251], s[26:27]
	s_add_u32 s26, s26, 0x2000
	s_addc_u32 s27, s27, 0
	ds_read_b128 v[244:247], v252 offset:2560
	ds_read_b128 v[248:251], v252 offset:3840
	s_waitcnt lgkmcnt(0)
	global_store_dwordx4 v223, v[244:247], s[26:27]
	s_add_u32 s26, s26, 0x2000
	s_addc_u32 s27, s27, 0
	s_nop 0
	global_store_dwordx4 v223, v[248:251], s[26:27]
.Lcv_next_0:
	s_add_i32 s98, s98, 1
.Lcv_done_0:
	s_cmp_ge_u32 s78, s74
	s_cbranch_scc1 .LBB0_577
	s_cmp_lt_u32 s78, s77
	s_cselect_b32 s18, 0, s77
	s_cselect_b32 s19, s76, s75
	s_lshl_b32 s18, s18, 6
	s_sub_i32 s25, s19, s18
	s_add_i32 s25, s25, s22
	v_add_u32_e32 v97, s25, v210
	v_mad_i64_i32 v[98:99], s[18:19], v97, s64, v[194:195]
	global_load_dwordx4 v[168:171], v[98:99], off
	s_and_saveexec_b64 s[18:19], s[0:1]
	s_cbranch_execz .LBB0_576
	v_add_u32_e32 v97, s25, v213
	v_mad_i64_i32 v[98:99], s[26:27], v97, s64, v[196:197]
	global_load_dwordx4 v[164:167], v[98:99], off
.LBB0_576:
	s_or_b64 exec, exec, s[18:19]
	s_ashr_i32 s18, s25, 6
	s_ashr_i32 s19, s18, 31
	s_lshl_b64 s[18:19], s[18:19], 16
	v_lshl_add_u64 v[98:99], v[198:199], 0, s[18:19]
	global_load_dwordx4 v[172:175], v[98:99], off
	global_load_dwordx4 v[244:247], v241, s[100:101] nt
	global_load_dwordx4 v[248:251], v242, s[100:101] nt

.LBB0_1058:
	s_add_i32 s1, s40, 0xffffff78
	s_lshl_b32 s0, s38, 3
	s_max_i32 s1, s1, 0
	s_mulk_i32 s1, 0x48
	s_add_i32 s0, s42, s0
	s_add_i32 s43, s0, s1
	s_cmpk_gt_i32 s43, 0x3fff
	s_mov_b32 s1, 0
	s_cbranch_scc1 .LBB0_1135
	s_lshl_b32 s44, s40, 3
	s_add_u32 s45, s10, 0x17458000
	s_mul_i32 s0, s42, 0x2400
	s_addc_u32 s46, s11, 0
	s_add_i32 s0, s0, 0
	s_add_u32 s47, s10, 0x7458000
	s_addc_u32 s48, s11, 0
	s_add_u32 s49, s10, 0x6458000
	s_addc_u32 s50, s11, 0
	s_add_u32 s51, s10, 0x5458000
	s_addc_u32 s52, s11, 0
	s_add_u32 s53, s10, 0x4d58000
	s_addc_u32 s54, s11, 0
	s_add_u32 s55, s10, 0x158000
	s_addc_u32 s56, s11, 0
	s_add_u32 s57, s10, 0x3390c000
	s_addc_u32 s58, s11, 0
	s_add_u32 s59, s10, 0x35e0c000
	v_lshlrev_b32_e32 v2, 1, v86
	v_and_b32_e32 v0, 60, v0
	v_and_b32_e32 v80, 48, v54
	s_addc_u32 s60, s11, 0
	v_and_b32_e32 v2, 0x60, v2
	v_and_b32_e32 v8, 7, v85
	v_lshrrev_b32_e32 v90, 3, v86
	v_mov_b32_e32 v79, 0
	v_add_u32_e32 v1, s0, v76
	v_mul_u32_u24_e32 v3, 0x50, v0
	v_add_u32_e32 v4, s0, v80
	v_mul_u32_u24_e32 v5, 0x50, v87
	s_add_u32 s61, s10, 0x3760c000
	v_add_u32_e32 v6, s0, v2
	v_mul_u32_u24_e32 v7, 0x90, v0
	v_lshlrev_b32_e32 v2, 3, v8
	v_lshl_add_u32 v8, v8, 4, s0
	v_mul_u32_u24_e32 v9, 0x90, v90
	v_mov_b32_e32 v81, v79
	v_or_b32_e32 v77, 16, v87
	v_or_b32_e32 v88, 32, v87
	v_or_b32_e32 v89, 48, v87
	s_addc_u32 s62, s11, 0
	v_or_b32_e32 v91, 8, v90
	v_or_b32_e32 v92, 16, v90
	v_or_b32_e32 v93, 24, v90
	v_or_b32_e32 v94, 32, v90
	v_or_b32_e32 v95, 40, v90
	v_or_b32_e32 v96, 48, v90
	v_or_b32_e32 v97, 56, v90
	s_add_i32 s63, 0, 0x204f8
	s_movk_i32 s64, 0x2000
	s_movk_i32 s65, 0x4000
	s_movk_i32 s66, 0x6000
	s_mov_b32 s67, 0x12000
	s_mov_b32 s68, 0xc3e00000
	v_add_u32_e32 v98, v1, v3
	v_add_u32_e32 v99, v4, v5
	s_movk_i32 s69, 0x3000
	s_movk_i32 s70, 0x5000
	s_movk_i32 s71, 0x7000
	s_add_i32 s72, 0, 0x204c0
	s_add_i32 s73, 0, 0x204b8
	s_add_i32 s74, 0, 0x204b0
	s_add_i32 s75, 0, 0x204a8
	s_add_i32 s76, 0, 0x20458
	s_add_i32 s77, 0, 0x20448
	s_add_i32 s78, 0, 0x20440
	s_mov_b32 s79, 0x9000
	s_mov_b32 s80, 0x1b000
	s_mov_b32 s81, 0x25000
	s_mov_b32 s82, 0x2e000
	s_mov_b32 s83, 0x37000
	s_mov_b32 s84, 0x41000
	s_mov_b32 s85, 0x4a000
	s_mov_b32 s86, 0x53000
	s_mov_b32 s87, 0x5d000
	s_mov_b32 s88, 0x66000
	s_mov_b32 s89, 0x6f000
	s_mov_b32 s90, 0x79000
	s_mov_b32 s91, 0x82000
	s_mov_b32 s92, 0x8b000
	v_add_u32_e32 v100, v6, v7
	v_lshlrev_b32_e32 v78, 1, v2
	v_lshlrev_b32_e32 v82, 2, v0
	v_mov_b32_e32 v101, 0x43e00000
	v_mov_b32_e32 v104, v79
	v_mov_b32_e32 v105, v79
	v_mov_b32_e32 v106, v79
	v_mov_b32_e32 v107, v79
	v_add_u32_e32 v102, v8, v9
	s_branch .LBB0_1062

.LBB0_1061:
	s_add_i32 s43, s43, s44
	s_cmpk_lt_i32 s43, 0x4000
	s_cbranch_scc0 .LBB0_1134

	.amdhsa_kernel _Z3fwd6Params
		.amdhsa_group_segment_fixed_size 0
		.amdhsa_private_segment_fixed_size 0
		.amdhsa_kernarg_size 536
		.amdhsa_user_sgpr_count 2
		.amdhsa_user_sgpr_dispatch_ptr 0
		.amdhsa_user_sgpr_queue_ptr 0
		.amdhsa_user_sgpr_kernarg_segment_ptr 1
		.amdhsa_user_sgpr_dispatch_id 0
		.amdhsa_user_sgpr_kernarg_preload_length 0
		.amdhsa_user_sgpr_kernarg_preload_offset 0
		.amdhsa_user_sgpr_private_segment_size 0
		.amdhsa_uses_dynamic_stack 0
		.amdhsa_enable_private_segment 0
		.amdhsa_system_sgpr_workgroup_id_x 1
		.amdhsa_system_sgpr_workgroup_id_y 0
		.amdhsa_system_sgpr_workgroup_id_z 0
		.amdhsa_system_sgpr_workgroup_info 0
		.amdhsa_system_vgpr_workitem_id 0
		.amdhsa_next_free_vgpr 256
		.amdhsa_next_free_sgpr 102
		.amdhsa_accum_offset 256
		.amdhsa_reserve_vcc 1
		.amdhsa_float_round_mode_32 0
		.amdhsa_float_round_mode_16_64 0
		.amdhsa_float_denorm_mode_32 3
		.amdhsa_float_denorm_mode_16_64 3
		.amdhsa_dx10_clamp 1
		.amdhsa_ieee_mode 1
		.amdhsa_fp16_overflow 0
		.amdhsa_tg_split 0
		.amdhsa_exception_fp_ieee_invalid_op 0
		.amdhsa_exception_fp_denorm_src 0
		.amdhsa_exception_fp_ieee_div_zero 0
		.amdhsa_exception_fp_ieee_overflow 0
		.amdhsa_exception_fp_ieee_underflow 0
		.amdhsa_exception_fp_ieee_inexact 0
		.amdhsa_exception_int_div_zero 0
	.end_amdhsa_kernel

amdhsa.kernels:
  - .agpr_count:     0
    .args:
      - .offset:         0
        .size:           280
        .value_kind:     by_value
      - .offset:         280
        .size:           4
        .value_kind:     hidden_block_count_x
      - .offset:         284
        .size:           4
        .value_kind:     hidden_block_count_y
      - .offset:         288
        .size:           4
        .value_kind:     hidden_block_count_z
      - .offset:         292
        .size:           2
        .value_kind:     hidden_group_size_x
      - .offset:         294
        .size:           2
        .value_kind:     hidden_group_size_y
      - .offset:         296
        .size:           2
        .value_kind:     hidden_group_size_z
      - .offset:         298
        .size:           2
        .value_kind:     hidden_remainder_x
      - .offset:         300
        .size:           2
        .value_kind:     hidden_remainder_y
      - .offset:         302
        .size:           2
        .value_kind:     hidden_remainder_z
      - .offset:         320
        .size:           8
        .value_kind:     hidden_global_offset_x
      - .offset:         328
        .size:           8
        .value_kind:     hidden_global_offset_y
      - .offset:         336
        .size:           8
        .value_kind:     hidden_global_offset_z
      - .offset:         344
        .size:           2
        .value_kind:     hidden_grid_dims
      - .offset:         400
        .size:           4
        .value_kind:     hidden_dynamic_lds_size
    .group_segment_fixed_size: 0
    .kernarg_segment_align: 8
    .kernarg_segment_size: 536
    .language:       OpenCL C
    .language_version:
      - 2
      - 0
    .max_flat_workgroup_size: 512
    .name:           _Z3fwd6Params
    .private_segment_fixed_size: 0
    .sgpr_count:     108
    .sgpr_spill_count: 5
    .symbol:         _Z3fwd6Params.kd
    .uniform_work_group_size: 1
    .uses_dynamic_stack: false
    .vgpr_count:     256
    .vgpr_spill_count: 0
    .wavefront_size: 64
